# code placement: the four hand-written gather loop heads aligned to 64-byte boundaries
# speedup vs baseline: 1.0053x; 1.0028x over previous
.LBB4_45:
	v_or_b32_e32 v17, 1, v31
	v_add_u32_e32 v14, s30, v17
	v_min_i32_e32 v14, 0x1869f, v14
	v_lshl_add_u32 v14, v14, 8, v26
	global_load_dwordx4 v[10:13], v14, s[24:25]
	s_mov_b64 s[28:29], exec
	s_movk_i32 s0, 0x4400
	v_subrev_u32_e32 v1, s20, v32
	v_lshl_add_u32 v1, v1, 2, s0
	v_lshl_add_u32 v16, v32, 8, v26
	v_cmp_lt_i32_e64 s[2:3], v32, v33
	v_add_u32_e32 v14, 1, v32
	v_cmp_lt_i32_e64 s[8:9], v14, v33
	s_mov_b64 exec, s[2:3]
	ds_read_b32 v18, v1
	ds_read_b32 v19, v1 offset:4096
	s_waitcnt lgkmcnt(0)
	v_lshl_add_u32 v18, v18, 9, v26
	v_lshl_add_u32 v19, v19, 8, v26
	global_load_dwordx4 v[34:37], v18, s[4:5] offset:256 nt
	global_load_dwordx4 v[20:23], v18, s[4:5] nt
	global_load_dwordx4 v[38:41], v19, s[24:25]
	ds_read_b32 v18, v1 offset:8
	ds_read_b32 v19, v1 offset:4104
	s_mov_b64 exec, s[8:9]
	ds_read_b32 v24, v1 offset:4
	ds_read_b32 v25, v1 offset:4100
	s_waitcnt lgkmcnt(0)
	v_lshl_add_u32 v24, v24, 9, v26
	v_lshl_add_u32 v25, v25, 8, v26
	global_load_dwordx4 v[50:53], v24, s[4:5] offset:256 nt
	global_load_dwordx4 v[46:49], v24, s[4:5] nt
	global_load_dwordx4 v[54:57], v25, s[24:25]
	ds_read_b32 v24, v1 offset:12
	ds_read_b32 v25, v1 offset:4108
	s_mov_b64 exec, s[28:29]
	s_cmp_eq_u64 s[2:3], 0
	s_cbranch_scc1 .Ll0_p1_empty
	s_waitcnt vmcnt(3)
	s_branch .Ll0_p1_body
	.p2align 6

.Ll0_p1_done:
	s_movk_i32 s2, 0x110
	v_cvt_pk_f16_f32 v21, v8, v9
	v_cvt_pk_f16_f32 v20, v6, v7
	v_cvt_pk_f16_f32 v19, v4, v5
	v_cvt_pk_f16_f32 v18, v2, v3
	v_mad_u32_u24 v14, v44, s2, v26
	ds_write_b128 v14, v[18:21]
	v_mov_b32_e32 v14, 0x6400
	v_lshl_or_b32 v14, v17, 2, v14
	ds_read2_b32 v[32:33], v14 offset1:1
	v_add_u32_e32 v14, s30, v17
	s_mov_b32 s2, 0x186a0
	v_cmp_gt_i32_e32 vcc, s2, v14
	v_cvt_f32_f16_e32 v2, v10
	v_cvt_f32_f16_sdwa v3, v10 dst_sel:DWORD dst_unused:UNUSED_PAD src0_sel:WORD_1
	v_cvt_f32_f16_e32 v4, v11
	v_cvt_f32_f16_sdwa v5, v11 dst_sel:DWORD dst_unused:UNUSED_PAD src0_sel:WORD_1
	v_cvt_f32_f16_e32 v6, v12
	v_cvt_f32_f16_sdwa v7, v12 dst_sel:DWORD dst_unused:UNUSED_PAD src0_sel:WORD_1
	v_cvt_f32_f16_e32 v8, v13
	v_cvt_f32_f16_sdwa v9, v13 dst_sel:DWORD dst_unused:UNUSED_PAD src0_sel:WORD_1
	v_pk_mul_f32 v[2:3], v[30:31], v[2:3] op_sel_hi:[0,1]
	v_pk_mul_f32 v[4:5], v[30:31], v[4:5] op_sel_hi:[0,1]
	v_pk_mul_f32 v[6:7], v[30:31], v[6:7] op_sel_hi:[0,1]
	v_pk_mul_f32 v[8:9], v[30:31], v[8:9] op_sel_hi:[0,1]
	v_cndmask_b32_e32 v2, 0, v2, vcc
	v_cndmask_b32_e32 v3, 0, v3, vcc
	v_cndmask_b32_e32 v4, 0, v4, vcc
	v_cndmask_b32_e32 v5, 0, v5, vcc
	v_cndmask_b32_e32 v6, 0, v6, vcc
	v_cndmask_b32_e32 v7, 0, v7, vcc
	v_cndmask_b32_e32 v8, 0, v8, vcc
	v_cndmask_b32_e32 v9, 0, v9, vcc
	s_waitcnt lgkmcnt(0)
	v_subrev_u32_e32 v1, s20, v32
	v_lshl_add_u32 v1, v1, 2, s0
	v_lshl_add_u32 v16, v32, 8, v26
	v_cmp_lt_i32_e64 s[2:3], v32, v33
	v_add_u32_e32 v14, 1, v32
	v_cmp_lt_i32_e64 s[8:9], v14, v33
	s_mov_b64 exec, s[2:3]
	ds_read_b32 v18, v1
	ds_read_b32 v19, v1 offset:4096
	s_waitcnt lgkmcnt(0)
	v_lshl_add_u32 v18, v18, 9, v26
	v_lshl_add_u32 v19, v19, 8, v26
	global_load_dwordx4 v[34:37], v18, s[4:5] offset:256 nt
	global_load_dwordx4 v[20:23], v18, s[4:5] nt
	global_load_dwordx4 v[38:41], v19, s[24:25]
	ds_read_b32 v18, v1 offset:8
	ds_read_b32 v19, v1 offset:4104
	s_mov_b64 exec, s[8:9]
	ds_read_b32 v24, v1 offset:4
	ds_read_b32 v25, v1 offset:4100
	s_waitcnt lgkmcnt(0)
	v_lshl_add_u32 v24, v24, 9, v26
	v_lshl_add_u32 v25, v25, 8, v26
	global_load_dwordx4 v[50:53], v24, s[4:5] offset:256 nt
	global_load_dwordx4 v[46:49], v24, s[4:5] nt
	global_load_dwordx4 v[54:57], v25, s[24:25]
	ds_read_b32 v24, v1 offset:12
	ds_read_b32 v25, v1 offset:4108
	s_mov_b64 exec, s[28:29]
	s_cmp_eq_u64 s[2:3], 0
	s_cbranch_scc1 .Ll0_p2_empty
	s_waitcnt vmcnt(3)
	s_branch .Ll0_p2_body
	.p2align 6

.LBB5_24:
	v_or_b32_e32 v46, 1, v35
	v_add_u32_e32 v46, s24, v46
	v_min_i32_e32 v46, 0x1869f, v46
	v_lshl_add_u32 v46, v46, 8, v26
	global_load_dwordx4 v[30:33], v46, s[4:5]
	s_mov_b64 s[22:23], exec
	s_movk_i32 s0, 0x2200
	v_sub_u32_e32 v27, v44, v28
	v_lshl_add_u32 v27, v27, 2, s0
	v_lshl_add_u32 v29, v44, 8, v26
	v_cmp_lt_i32_e64 s[2:3], v44, v45
	v_add_u32_e32 v46, 1, v44
	v_cmp_lt_i32_e64 s[16:17], v46, v45
	v_add_u32_e32 v46, 2, v44
	v_cmp_lt_i32_e64 s[18:19], v46, v45
	v_add_u32_e32 v46, 3, v44
	v_cmp_lt_i32_e64 s[20:21], v46, v45
	s_mov_b64 exec, s[2:3]
	ds_read_b32 v2, v27 offset:0
	global_load_dwordx4 v[4:7], v29, s[12:13] offset:0
	s_waitcnt lgkmcnt(0)
	v_lshl_add_u32 v2, v2, 8, v26
	global_load_dwordx4 v[8:11], v2, s[4:5]
	ds_read_b32 v2, v27 offset:16
	s_mov_b64 exec, s[16:17]
	ds_read_b32 v3, v27 offset:4
	global_load_dwordx4 v[12:15], v29, s[12:13] offset:256
	s_waitcnt lgkmcnt(0)
	v_lshl_add_u32 v3, v3, 8, v26
	global_load_dwordx4 v[16:19], v3, s[4:5]
	ds_read_b32 v3, v27 offset:20
	s_mov_b64 exec, s[18:19]
	ds_read_b32 v24, v27 offset:8
	global_load_dwordx4 v[20:23], v29, s[12:13] offset:512
	s_waitcnt lgkmcnt(0)
	v_lshl_add_u32 v24, v24, 8, v26
	global_load_dwordx4 v[50:53], v24, s[4:5]
	ds_read_b32 v24, v27 offset:24
	s_mov_b64 exec, s[20:21]
	ds_read_b32 v25, v27 offset:12
	global_load_dwordx4 v[54:57], v29, s[12:13] offset:768
	s_waitcnt lgkmcnt(0)
	v_lshl_add_u32 v25, v25, 8, v26
	global_load_dwordx4 v[58:61], v25, s[4:5]
	ds_read_b32 v25, v27 offset:28
	s_mov_b64 exec, s[22:23]
	s_cmp_eq_u64 s[2:3], 0
	s_cbranch_scc1 .Ll1_p1_empty
	.p2align 6

.Ll1_p1_done:
	s_movk_i32 s2, 0x110
	v_cvt_pk_f16_f32 v5, v36, v37
	v_cvt_pk_f16_f32 v4, v38, v39
	v_cvt_pk_f16_f32 v3, v40, v41
	v_cvt_pk_f16_f32 v2, v42, v43
	v_and_b32_e32 v46, 30, v35
	v_mad_u32_u24 v46, v46, s2, v26
	ds_write_b128 v46, v[2:5]
	v_or_b32_e32 v47, 1, v35
	v_mov_b32_e32 v46, 0x3200
	v_lshl_or_b32 v46, v47, 2, v46
	ds_read2_b32 v[44:45], v46 offset1:1
	v_add_u32_e32 v46, s24, v47
	s_mov_b32 s2, 0x186a0
	v_cmp_gt_i32_e32 vcc, s2, v46
	v_cvt_f32_f16_e32 v42, v30
	v_cvt_f32_f16_sdwa v43, v30 dst_sel:DWORD dst_unused:UNUSED_PAD src0_sel:WORD_1
	v_cvt_f32_f16_e32 v40, v31
	v_cvt_f32_f16_sdwa v41, v31 dst_sel:DWORD dst_unused:UNUSED_PAD src0_sel:WORD_1
	v_cvt_f32_f16_e32 v38, v32
	v_cvt_f32_f16_sdwa v39, v32 dst_sel:DWORD dst_unused:UNUSED_PAD src0_sel:WORD_1
	v_cvt_f32_f16_e32 v36, v33
	v_cvt_f32_f16_sdwa v37, v33 dst_sel:DWORD dst_unused:UNUSED_PAD src0_sel:WORD_1
	v_mul_f32_e32 v36, v34, v36
	v_mul_f32_e32 v37, v34, v37
	v_mul_f32_e32 v38, v34, v38
	v_mul_f32_e32 v39, v34, v39
	v_mul_f32_e32 v40, v34, v40
	v_mul_f32_e32 v41, v34, v41
	v_mul_f32_e32 v42, v34, v42
	v_mul_f32_e32 v43, v34, v43
	v_cndmask_b32_e32 v36, 0, v36, vcc
	v_cndmask_b32_e32 v37, 0, v37, vcc
	v_cndmask_b32_e32 v38, 0, v38, vcc
	v_cndmask_b32_e32 v39, 0, v39, vcc
	v_cndmask_b32_e32 v40, 0, v40, vcc
	v_cndmask_b32_e32 v41, 0, v41, vcc
	v_cndmask_b32_e32 v42, 0, v42, vcc
	v_cndmask_b32_e32 v43, 0, v43, vcc
	s_waitcnt lgkmcnt(0)
	v_sub_u32_e32 v27, v44, v28
	v_lshl_add_u32 v27, v27, 2, s0
	v_lshl_add_u32 v29, v44, 8, v26
	v_cmp_lt_i32_e64 s[2:3], v44, v45
	v_add_u32_e32 v46, 1, v44
	v_cmp_lt_i32_e64 s[16:17], v46, v45
	v_add_u32_e32 v46, 2, v44
	v_cmp_lt_i32_e64 s[18:19], v46, v45
	v_add_u32_e32 v46, 3, v44
	v_cmp_lt_i32_e64 s[20:21], v46, v45
	s_mov_b64 exec, s[2:3]
	ds_read_b32 v2, v27 offset:0
	global_load_dwordx4 v[4:7], v29, s[12:13] offset:0
	s_waitcnt lgkmcnt(0)
	v_lshl_add_u32 v2, v2, 8, v26
	global_load_dwordx4 v[8:11], v2, s[4:5]
	ds_read_b32 v2, v27 offset:16
	s_mov_b64 exec, s[16:17]
	ds_read_b32 v3, v27 offset:4
	global_load_dwordx4 v[12:15], v29, s[12:13] offset:256
	s_waitcnt lgkmcnt(0)
	v_lshl_add_u32 v3, v3, 8, v26
	global_load_dwordx4 v[16:19], v3, s[4:5]
	ds_read_b32 v3, v27 offset:20
	s_mov_b64 exec, s[18:19]
	ds_read_b32 v24, v27 offset:8
	global_load_dwordx4 v[20:23], v29, s[12:13] offset:512
	s_waitcnt lgkmcnt(0)
	v_lshl_add_u32 v24, v24, 8, v26
	global_load_dwordx4 v[50:53], v24, s[4:5]
	ds_read_b32 v24, v27 offset:24
	s_mov_b64 exec, s[20:21]
	ds_read_b32 v25, v27 offset:12
	global_load_dwordx4 v[54:57], v29, s[12:13] offset:768
	s_waitcnt lgkmcnt(0)
	v_lshl_add_u32 v25, v25, 8, v26
	global_load_dwordx4 v[58:61], v25, s[4:5]
	ds_read_b32 v25, v27 offset:28
	s_mov_b64 exec, s[22:23]
	s_cmp_eq_u64 s[2:3], 0
	s_cbranch_scc1 .Ll1_p2_empty
	.p2align 6
